# MoE up-projection epilogue: silu(a)*b with packed f32 multiplies/adds (same per-element arithmetic), on top of the MLA loop changes
# speedup vs baseline: 1.0223x; 1.0113x over previous
; __device__ __forceinline__ u32x4 pack8(const f32x4 a, const f32x4 b) { u32x4 w; w.x = cvt_pk_bf16(a[0], a[1]); w.y = cvt_pk_bf16(a[2], a[3]); w.z = cvt_pk_bf16(b[0], b[1]); w.w = cvt_pk_bf16(b[2], b[3]); return w; }
; __device__ __forceinline__ float silu_f(float x) { return x * __builtin_amdgcn_rcpf(1.0f + __builtin_amdgcn_exp2f(-1.4426950409f * x)); }
;     w = __builtin_amdgcn_cvt_pk_fp8_f32(__builtin_amdgcn_fmed3f(v[2] * 8.0f, -448.0f, 448.0f), __builtin_amdgcn_fmed3f(v[3] * 8.0f, -448.0f, 448.0f), w, true); return (unsigned)w; }
;     __device__ __forceinline__ void operator()(const f32x4 (&acc)[2][2][4][2], const Unit& u, int wr, int wc, int fr, int fq) const {
;     ...
;         for (int ai = 0; ai < 2; ++ai)
; #pragma unroll
;             for (int m = 0; m < 4; ++m) {
;                 const float r = rs[ai][m]; f32x4 o[2];
; #pragma unroll
;                 for (int n = 0; n < 2; ++n) { const f32x4 a = acc[ai][0][m][n] * r, b = acc[ai][1][m][n] * r;
;                     o[n] = (f32x4){silu_f(a[0]) * b[0], silu_f(a[1]) * b[1], silu_f(a[2]) * b[2], silu_f(a[3]) * b[3]}; }
;                 if (F8OUT) { u32x2 w; w.x = pack4_fp8(o[0]); w.y = pack4_fp8(o[1]); *(u32x2*)((unsigned char*)h + (size_t)(row0 + ai * HALF + m * 16) * FFN + col0) = w; }
;                 else *(u32x4*)(h + (size_t)(row0 + ai * HALF + m * 16) * FFN + col0) = pack8(o[0], o[1]);
.LBB0_1375:
	v_mov_b32_e32 v14, 0xbfb8aa3b
	v_mov_b32_e32 v16, 0x41000000
	v_mov_b32_e32 v20, 1.0
	v_pk_mul_f32 v[4:5], v[154:155], v[14:15] op_sel_hi:[1,0]
	v_pk_mul_f32 v[6:7], v[156:157], v[14:15] op_sel_hi:[1,0]
	v_pk_mul_f32 v[8:9], v[150:151], v[14:15] op_sel_hi:[1,0]
	v_pk_mul_f32 v[10:11], v[152:153], v[14:15] op_sel_hi:[1,0]
	v_exp_f32_e32 v4, v4
	v_exp_f32_e32 v5, v5
	v_exp_f32_e32 v6, v6
	v_exp_f32_e32 v7, v7
	v_exp_f32_e32 v8, v8
	v_exp_f32_e32 v9, v9
	v_exp_f32_e32 v10, v10
	v_exp_f32_e32 v11, v11
	v_pk_add_f32 v[4:5], v[4:5], v[20:21] op_sel_hi:[1,0]
	v_pk_add_f32 v[6:7], v[6:7], v[20:21] op_sel_hi:[1,0]
	v_pk_add_f32 v[8:9], v[8:9], v[20:21] op_sel_hi:[1,0]
	v_pk_add_f32 v[10:11], v[10:11], v[20:21] op_sel_hi:[1,0]
	v_rcp_f32_e32 v4, v4
	v_rcp_f32_e32 v5, v5
	v_rcp_f32_e32 v6, v6
	v_rcp_f32_e32 v7, v7
	v_rcp_f32_e32 v8, v8
	v_rcp_f32_e32 v9, v9
	v_rcp_f32_e32 v10, v10
	v_rcp_f32_e32 v11, v11
	v_pk_mul_f32 v[4:5], v[154:155], v[4:5]
	v_pk_mul_f32 v[6:7], v[156:157], v[6:7]
	v_pk_mul_f32 v[8:9], v[150:151], v[8:9]
	v_pk_mul_f32 v[10:11], v[152:153], v[10:11]
	v_pk_mul_f32 v[4:5], v[158:159], v[4:5]
	v_pk_mul_f32 v[6:7], v[160:161], v[6:7]
	v_pk_mul_f32 v[8:9], v[146:147], v[8:9]
	v_pk_mul_f32 v[10:11], v[148:149], v[10:11]
	v_pk_mul_f32 v[4:5], v[4:5], v[16:17] op_sel_hi:[1,0]
	v_pk_mul_f32 v[6:7], v[6:7], v[16:17] op_sel_hi:[1,0]
	v_pk_mul_f32 v[8:9], v[8:9], v[16:17] op_sel_hi:[1,0]
	v_pk_mul_f32 v[10:11], v[10:11], v[16:17] op_sel_hi:[1,0]
	v_med3_f32 v4, v4, s64, v250
	v_med3_f32 v5, v5, s64, v250
	v_med3_f32 v6, v6, s64, v250
	v_med3_f32 v7, v7, s64, v250
	v_med3_f32 v8, v8, s64, v250
	v_med3_f32 v9, v9, s64, v250
	v_med3_f32 v10, v10, s64, v250
	v_med3_f32 v11, v11, s64, v250
	v_cvt_pk_fp8_f32 v12, v4, v5
	v_cvt_pk_fp8_f32 v13, v8, v9
	s_nop 0
	v_cvt_pk_fp8_f32 v12, v6, v7 op_sel:[0,0,1]
	v_cvt_pk_fp8_f32 v13, v10, v11 op_sel:[0,0,1]
	v_lshl_or_b32 v2, s62, 7, v193
	v_ashrrev_i32_e32 v3, 31, v2
	v_lshl_add_u32 v0, s63, 8, v163
	v_lshl_add_u64 v[2:3], s[20:21], 0, v[2:3]
	s_nop 15
	s_nop 15
	v_mad_i64_i32 v[18:19], s[22:23], v0, s73, v[2:3]
	s_waitcnt vmcnt(0)
	global_store_dwordx2 v[18:19], v[12:13], off
	v_pk_mul_f32 v[4:5], v[142:143], v[14:15] op_sel_hi:[1,0]
	v_pk_mul_f32 v[6:7], v[144:145], v[14:15] op_sel_hi:[1,0]
	v_pk_mul_f32 v[8:9], v[134:135], v[14:15] op_sel_hi:[1,0]
	v_pk_mul_f32 v[10:11], v[136:137], v[14:15] op_sel_hi:[1,0]
	v_exp_f32_e32 v4, v4
	v_exp_f32_e32 v5, v5
	v_exp_f32_e32 v6, v6
	v_exp_f32_e32 v7, v7
	v_exp_f32_e32 v8, v8
	v_exp_f32_e32 v9, v9
	v_exp_f32_e32 v10, v10
	v_exp_f32_e32 v11, v11
	v_pk_add_f32 v[4:5], v[4:5], v[20:21] op_sel_hi:[1,0]
	v_pk_add_f32 v[6:7], v[6:7], v[20:21] op_sel_hi:[1,0]
	v_pk_add_f32 v[8:9], v[8:9], v[20:21] op_sel_hi:[1,0]
	v_pk_add_f32 v[10:11], v[10:11], v[20:21] op_sel_hi:[1,0]
	v_rcp_f32_e32 v4, v4
	v_rcp_f32_e32 v5, v5
	v_rcp_f32_e32 v6, v6
	v_rcp_f32_e32 v7, v7
	v_rcp_f32_e32 v8, v8
	v_rcp_f32_e32 v9, v9
	v_rcp_f32_e32 v10, v10
	v_rcp_f32_e32 v11, v11
	v_pk_mul_f32 v[4:5], v[142:143], v[4:5]
	v_pk_mul_f32 v[6:7], v[144:145], v[6:7]
	v_pk_mul_f32 v[8:9], v[134:135], v[8:9]
	v_pk_mul_f32 v[10:11], v[136:137], v[10:11]
	v_pk_mul_f32 v[4:5], v[138:139], v[4:5]
	v_pk_mul_f32 v[6:7], v[140:141], v[6:7]
	v_pk_mul_f32 v[8:9], v[130:131], v[8:9]
	v_pk_mul_f32 v[10:11], v[132:133], v[10:11]
	v_pk_mul_f32 v[4:5], v[4:5], v[16:17] op_sel_hi:[1,0]
	v_pk_mul_f32 v[6:7], v[6:7], v[16:17] op_sel_hi:[1,0]
	v_pk_mul_f32 v[8:9], v[8:9], v[16:17] op_sel_hi:[1,0]
	v_pk_mul_f32 v[10:11], v[10:11], v[16:17] op_sel_hi:[1,0]
	v_med3_f32 v4, v4, s64, v250
	v_med3_f32 v5, v5, s64, v250
	v_med3_f32 v6, v6, s64, v250
	v_med3_f32 v7, v7, s64, v250
	v_med3_f32 v8, v8, s64, v250
	v_med3_f32 v9, v9, s64, v250
	v_med3_f32 v10, v10, s64, v250
	v_med3_f32 v11, v11, s64, v250
	v_cvt_pk_fp8_f32 v12, v4, v5
	v_cvt_pk_fp8_f32 v13, v8, v9
	s_nop 0
	v_cvt_pk_fp8_f32 v12, v6, v7 op_sel:[0,0,1]
	v_cvt_pk_fp8_f32 v13, v10, v11 op_sel:[0,0,1]
	v_or_b32_e32 v18, 16, v0
	v_mad_i64_i32 v[18:19], s[22:23], v18, s73, v[2:3]
	global_store_dwordx2 v[18:19], v[12:13], off
	v_pk_mul_f32 v[4:5], v[126:127], v[14:15] op_sel_hi:[1,0]
	v_pk_mul_f32 v[6:7], v[128:129], v[14:15] op_sel_hi:[1,0]
	v_pk_mul_f32 v[8:9], v[118:119], v[14:15] op_sel_hi:[1,0]
	v_pk_mul_f32 v[10:11], v[120:121], v[14:15] op_sel_hi:[1,0]
	v_exp_f32_e32 v4, v4
	v_exp_f32_e32 v5, v5
	v_exp_f32_e32 v6, v6
	v_exp_f32_e32 v7, v7
	v_exp_f32_e32 v8, v8
	v_exp_f32_e32 v9, v9
	v_exp_f32_e32 v10, v10
	v_exp_f32_e32 v11, v11
	v_pk_add_f32 v[4:5], v[4:5], v[20:21] op_sel_hi:[1,0]
	v_pk_add_f32 v[6:7], v[6:7], v[20:21] op_sel_hi:[1,0]
	v_pk_add_f32 v[8:9], v[8:9], v[20:21] op_sel_hi:[1,0]
	v_pk_add_f32 v[10:11], v[10:11], v[20:21] op_sel_hi:[1,0]
	v_rcp_f32_e32 v4, v4
	v_rcp_f32_e32 v5, v5
	v_rcp_f32_e32 v6, v6
	v_rcp_f32_e32 v7, v7
	v_rcp_f32_e32 v8, v8
	v_rcp_f32_e32 v9, v9
	v_rcp_f32_e32 v10, v10
	v_rcp_f32_e32 v11, v11
	v_pk_mul_f32 v[4:5], v[126:127], v[4:5]
	v_pk_mul_f32 v[6:7], v[128:129], v[6:7]
	v_pk_mul_f32 v[8:9], v[118:119], v[8:9]
	v_pk_mul_f32 v[10:11], v[120:121], v[10:11]
	v_pk_mul_f32 v[4:5], v[122:123], v[4:5]
	v_pk_mul_f32 v[6:7], v[124:125], v[6:7]
	v_pk_mul_f32 v[8:9], v[114:115], v[8:9]
	v_pk_mul_f32 v[10:11], v[116:117], v[10:11]
	v_pk_mul_f32 v[4:5], v[4:5], v[16:17] op_sel_hi:[1,0]
	v_pk_mul_f32 v[6:7], v[6:7], v[16:17] op_sel_hi:[1,0]
	v_pk_mul_f32 v[8:9], v[8:9], v[16:17] op_sel_hi:[1,0]
	v_pk_mul_f32 v[10:11], v[10:11], v[16:17] op_sel_hi:[1,0]
	v_med3_f32 v4, v4, s64, v250
	v_med3_f32 v5, v5, s64, v250
	v_med3_f32 v6, v6, s64, v250
	v_med3_f32 v7, v7, s64, v250
	v_med3_f32 v8, v8, s64, v250
	v_med3_f32 v9, v9, s64, v250
; __device__ __forceinline__ u32x4 pack8(const f32x4 a, const f32x4 b) { u32x4 w; w.x = cvt_pk_bf16(a[0], a[1]); w.y = cvt_pk_bf16(a[2], a[3]); w.z = cvt_pk_bf16(b[0], b[1]); w.w = cvt_pk_bf16(b[2], b[3]); return w; }
; __device__ __forceinline__ float silu_f(float x) { return x * __builtin_amdgcn_rcpf(1.0f + __builtin_amdgcn_exp2f(-1.4426950409f * x)); }
;     w = __builtin_amdgcn_cvt_pk_fp8_f32(__builtin_amdgcn_fmed3f(v[2] * 8.0f, -448.0f, 448.0f), __builtin_amdgcn_fmed3f(v[3] * 8.0f, -448.0f, 448.0f), w, true); return (unsigned)w; }
;     __device__ __forceinline__ void operator()(const f32x4 (&acc)[2][2][4][2], const Unit& u, int wr, int wc, int fr, int fq) const {
;     ...
;         for (int ai = 0; ai < 2; ++ai)
; #pragma unroll
;             for (int m = 0; m < 4; ++m) {
;                 const float r = rs[ai][m]; f32x4 o[2];
; #pragma unroll
;                 for (int n = 0; n < 2; ++n) { const f32x4 a = acc[ai][0][m][n] * r, b = acc[ai][1][m][n] * r;
;                     o[n] = (f32x4){silu_f(a[0]) * b[0], silu_f(a[1]) * b[1], silu_f(a[2]) * b[2], silu_f(a[3]) * b[3]}; }
;                 if (F8OUT) { u32x2 w; w.x = pack4_fp8(o[0]); w.y = pack4_fp8(o[1]); *(u32x2*)((unsigned char*)h + (size_t)(row0 + ai * HALF + m * 16) * FFN + col0) = w; }
;                 else *(u32x4*)(h + (size_t)(row0 + ai * HALF + m * 16) * FFN + col0) = pack8(o[0], o[1]);
	v_med3_f32 v10, v10, s64, v250
	v_med3_f32 v11, v11, s64, v250
	v_cvt_pk_fp8_f32 v12, v4, v5
	v_cvt_pk_fp8_f32 v13, v8, v9
	s_nop 0
	v_cvt_pk_fp8_f32 v12, v6, v7 op_sel:[0,0,1]
	v_cvt_pk_fp8_f32 v13, v10, v11 op_sel:[0,0,1]
	v_or_b32_e32 v18, 32, v0
	v_mad_i64_i32 v[18:19], s[22:23], v18, s73, v[2:3]
	global_store_dwordx2 v[18:19], v[12:13], off
	v_pk_mul_f32 v[4:5], v[110:111], v[14:15] op_sel_hi:[1,0]
	v_pk_mul_f32 v[6:7], v[112:113], v[14:15] op_sel_hi:[1,0]
	v_pk_mul_f32 v[8:9], v[102:103], v[14:15] op_sel_hi:[1,0]
	v_pk_mul_f32 v[10:11], v[104:105], v[14:15] op_sel_hi:[1,0]
	v_exp_f32_e32 v4, v4
	v_exp_f32_e32 v5, v5
	v_exp_f32_e32 v6, v6
	v_exp_f32_e32 v7, v7
	v_exp_f32_e32 v8, v8
	v_exp_f32_e32 v9, v9
	v_exp_f32_e32 v10, v10
	v_exp_f32_e32 v11, v11
	v_pk_add_f32 v[4:5], v[4:5], v[20:21] op_sel_hi:[1,0]
	v_pk_add_f32 v[6:7], v[6:7], v[20:21] op_sel_hi:[1,0]
	v_pk_add_f32 v[8:9], v[8:9], v[20:21] op_sel_hi:[1,0]
	v_pk_add_f32 v[10:11], v[10:11], v[20:21] op_sel_hi:[1,0]
	v_rcp_f32_e32 v4, v4
	v_rcp_f32_e32 v5, v5
	v_rcp_f32_e32 v6, v6
	v_rcp_f32_e32 v7, v7
	v_rcp_f32_e32 v8, v8
	v_rcp_f32_e32 v9, v9
	v_rcp_f32_e32 v10, v10
	v_rcp_f32_e32 v11, v11
	v_pk_mul_f32 v[4:5], v[110:111], v[4:5]
	v_pk_mul_f32 v[6:7], v[112:113], v[6:7]
	v_pk_mul_f32 v[8:9], v[102:103], v[8:9]
	v_pk_mul_f32 v[10:11], v[104:105], v[10:11]
	v_pk_mul_f32 v[4:5], v[106:107], v[4:5]
	v_pk_mul_f32 v[6:7], v[108:109], v[6:7]
	v_pk_mul_f32 v[8:9], v[98:99], v[8:9]
	v_pk_mul_f32 v[10:11], v[100:101], v[10:11]
	v_pk_mul_f32 v[4:5], v[4:5], v[16:17] op_sel_hi:[1,0]
	v_pk_mul_f32 v[6:7], v[6:7], v[16:17] op_sel_hi:[1,0]
	v_pk_mul_f32 v[8:9], v[8:9], v[16:17] op_sel_hi:[1,0]
	v_pk_mul_f32 v[10:11], v[10:11], v[16:17] op_sel_hi:[1,0]
	v_med3_f32 v4, v4, s64, v250
	v_med3_f32 v5, v5, s64, v250
	v_med3_f32 v6, v6, s64, v250
	v_med3_f32 v7, v7, s64, v250
	v_med3_f32 v8, v8, s64, v250
	v_med3_f32 v9, v9, s64, v250
	v_med3_f32 v10, v10, s64, v250
	v_med3_f32 v11, v11, s64, v250
	v_cvt_pk_fp8_f32 v12, v4, v5
	v_cvt_pk_fp8_f32 v13, v8, v9
	s_nop 0
	v_cvt_pk_fp8_f32 v12, v6, v7 op_sel:[0,0,1]
	v_cvt_pk_fp8_f32 v13, v10, v11 op_sel:[0,0,1]
	v_or_b32_e32 v18, 48, v0
	v_mad_i64_i32 v[18:19], s[22:23], v18, s73, v[2:3]
	global_store_dwordx2 v[18:19], v[12:13], off
	v_pk_mul_f32 v[4:5], v[94:95], v[14:15] op_sel_hi:[1,0]
	v_pk_mul_f32 v[6:7], v[96:97], v[14:15] op_sel_hi:[1,0]
	v_pk_mul_f32 v[8:9], v[86:87], v[14:15] op_sel_hi:[1,0]
	v_pk_mul_f32 v[10:11], v[88:89], v[14:15] op_sel_hi:[1,0]
	v_exp_f32_e32 v4, v4
	v_exp_f32_e32 v5, v5
	v_exp_f32_e32 v6, v6
	v_exp_f32_e32 v7, v7
	v_exp_f32_e32 v8, v8
	v_exp_f32_e32 v9, v9
	v_exp_f32_e32 v10, v10
	v_exp_f32_e32 v11, v11
	v_pk_add_f32 v[4:5], v[4:5], v[20:21] op_sel_hi:[1,0]
	v_pk_add_f32 v[6:7], v[6:7], v[20:21] op_sel_hi:[1,0]
	v_pk_add_f32 v[8:9], v[8:9], v[20:21] op_sel_hi:[1,0]
	v_pk_add_f32 v[10:11], v[10:11], v[20:21] op_sel_hi:[1,0]
	v_rcp_f32_e32 v4, v4
	v_rcp_f32_e32 v5, v5
	v_rcp_f32_e32 v6, v6
	v_rcp_f32_e32 v7, v7
	v_rcp_f32_e32 v8, v8
	v_rcp_f32_e32 v9, v9
	v_rcp_f32_e32 v10, v10
	v_rcp_f32_e32 v11, v11
	v_pk_mul_f32 v[4:5], v[94:95], v[4:5]
	v_pk_mul_f32 v[6:7], v[96:97], v[6:7]
	v_pk_mul_f32 v[8:9], v[86:87], v[8:9]
	v_pk_mul_f32 v[10:11], v[88:89], v[10:11]
	v_pk_mul_f32 v[4:5], v[90:91], v[4:5]
	v_pk_mul_f32 v[6:7], v[92:93], v[6:7]
	v_pk_mul_f32 v[8:9], v[82:83], v[8:9]
	v_pk_mul_f32 v[10:11], v[84:85], v[10:11]
	v_pk_mul_f32 v[4:5], v[4:5], v[16:17] op_sel_hi:[1,0]
	v_pk_mul_f32 v[6:7], v[6:7], v[16:17] op_sel_hi:[1,0]
	v_pk_mul_f32 v[8:9], v[8:9], v[16:17] op_sel_hi:[1,0]
	v_pk_mul_f32 v[10:11], v[10:11], v[16:17] op_sel_hi:[1,0]
	v_med3_f32 v4, v4, s64, v250
	v_med3_f32 v5, v5, s64, v250
	v_med3_f32 v6, v6, s64, v250
	v_med3_f32 v7, v7, s64, v250
	v_med3_f32 v8, v8, s64, v250
	v_med3_f32 v9, v9, s64, v250
	v_med3_f32 v10, v10, s64, v250
	v_med3_f32 v11, v11, s64, v250
	v_cvt_pk_fp8_f32 v12, v4, v5
	v_cvt_pk_fp8_f32 v13, v8, v9
	s_nop 0
	v_cvt_pk_fp8_f32 v12, v6, v7 op_sel:[0,0,1]
	v_cvt_pk_fp8_f32 v13, v10, v11 op_sel:[0,0,1]
	v_add_u32_e32 v18, 0x80, v0
	v_mad_i64_i32 v[18:19], s[22:23], v18, s73, v[2:3]
	global_store_dwordx2 v[18:19], v[12:13], off
	v_pk_mul_f32 v[4:5], v[78:79], v[14:15] op_sel_hi:[1,0]
	v_pk_mul_f32 v[6:7], v[80:81], v[14:15] op_sel_hi:[1,0]
	v_pk_mul_f32 v[8:9], v[70:71], v[14:15] op_sel_hi:[1,0]
	v_pk_mul_f32 v[10:11], v[72:73], v[14:15] op_sel_hi:[1,0]
	v_exp_f32_e32 v4, v4
	v_exp_f32_e32 v5, v5
	v_exp_f32_e32 v6, v6
	v_exp_f32_e32 v7, v7
	v_exp_f32_e32 v8, v8
	v_exp_f32_e32 v9, v9
	v_exp_f32_e32 v10, v10
	v_exp_f32_e32 v11, v11
	v_pk_add_f32 v[4:5], v[4:5], v[20:21] op_sel_hi:[1,0]
	v_pk_add_f32 v[6:7], v[6:7], v[20:21] op_sel_hi:[1,0]
	v_pk_add_f32 v[8:9], v[8:9], v[20:21] op_sel_hi:[1,0]
	v_pk_add_f32 v[10:11], v[10:11], v[20:21] op_sel_hi:[1,0]
	v_rcp_f32_e32 v4, v4
	v_rcp_f32_e32 v5, v5
	v_rcp_f32_e32 v6, v6
	v_rcp_f32_e32 v7, v7
	v_rcp_f32_e32 v8, v8
	v_rcp_f32_e32 v9, v9
	v_rcp_f32_e32 v10, v10
	v_rcp_f32_e32 v11, v11
	v_pk_mul_f32 v[4:5], v[78:79], v[4:5]
; __device__ __forceinline__ u32x4 pack8(const f32x4 a, const f32x4 b) { u32x4 w; w.x = cvt_pk_bf16(a[0], a[1]); w.y = cvt_pk_bf16(a[2], a[3]); w.z = cvt_pk_bf16(b[0], b[1]); w.w = cvt_pk_bf16(b[2], b[3]); return w; }
; __device__ __forceinline__ float silu_f(float x) { return x * __builtin_amdgcn_rcpf(1.0f + __builtin_amdgcn_exp2f(-1.4426950409f * x)); }
;     w = __builtin_amdgcn_cvt_pk_fp8_f32(__builtin_amdgcn_fmed3f(v[2] * 8.0f, -448.0f, 448.0f), __builtin_amdgcn_fmed3f(v[3] * 8.0f, -448.0f, 448.0f), w, true); return (unsigned)w; }
;     __device__ __forceinline__ void operator()(const f32x4 (&acc)[2][2][4][2], const Unit& u, int wr, int wc, int fr, int fq) const {
;     ...
;         for (int ai = 0; ai < 2; ++ai)
; #pragma unroll
;             for (int m = 0; m < 4; ++m) {
;                 const float r = rs[ai][m]; f32x4 o[2];
; #pragma unroll
;                 for (int n = 0; n < 2; ++n) { const f32x4 a = acc[ai][0][m][n] * r, b = acc[ai][1][m][n] * r;
;                     o[n] = (f32x4){silu_f(a[0]) * b[0], silu_f(a[1]) * b[1], silu_f(a[2]) * b[2], silu_f(a[3]) * b[3]}; }
;                 if (F8OUT) { u32x2 w; w.x = pack4_fp8(o[0]); w.y = pack4_fp8(o[1]); *(u32x2*)((unsigned char*)h + (size_t)(row0 + ai * HALF + m * 16) * FFN + col0) = w; }
;                 else *(u32x4*)(h + (size_t)(row0 + ai * HALF + m * 16) * FFN + col0) = pack8(o[0], o[1]);
	v_pk_mul_f32 v[6:7], v[80:81], v[6:7]
	v_pk_mul_f32 v[8:9], v[70:71], v[8:9]
	v_pk_mul_f32 v[10:11], v[72:73], v[10:11]
	v_pk_mul_f32 v[4:5], v[74:75], v[4:5]
	v_pk_mul_f32 v[6:7], v[76:77], v[6:7]
	v_pk_mul_f32 v[8:9], v[66:67], v[8:9]
	v_pk_mul_f32 v[10:11], v[68:69], v[10:11]
	v_pk_mul_f32 v[4:5], v[4:5], v[16:17] op_sel_hi:[1,0]
	v_pk_mul_f32 v[6:7], v[6:7], v[16:17] op_sel_hi:[1,0]
	v_pk_mul_f32 v[8:9], v[8:9], v[16:17] op_sel_hi:[1,0]
	v_pk_mul_f32 v[10:11], v[10:11], v[16:17] op_sel_hi:[1,0]
	v_med3_f32 v4, v4, s64, v250
	v_med3_f32 v5, v5, s64, v250
	v_med3_f32 v6, v6, s64, v250
	v_med3_f32 v7, v7, s64, v250
	v_med3_f32 v8, v8, s64, v250
	v_med3_f32 v9, v9, s64, v250
	v_med3_f32 v10, v10, s64, v250
	v_med3_f32 v11, v11, s64, v250
	v_cvt_pk_fp8_f32 v12, v4, v5
	v_cvt_pk_fp8_f32 v13, v8, v9
	s_nop 0
	v_cvt_pk_fp8_f32 v12, v6, v7 op_sel:[0,0,1]
	v_cvt_pk_fp8_f32 v13, v10, v11 op_sel:[0,0,1]
	v_add_u32_e32 v18, 0x90, v0
	v_mad_i64_i32 v[18:19], s[22:23], v18, s73, v[2:3]
	global_store_dwordx2 v[18:19], v[12:13], off
	v_pk_mul_f32 v[4:5], v[62:63], v[14:15] op_sel_hi:[1,0]
	v_pk_mul_f32 v[6:7], v[64:65], v[14:15] op_sel_hi:[1,0]
	v_pk_mul_f32 v[8:9], v[54:55], v[14:15] op_sel_hi:[1,0]
	v_pk_mul_f32 v[10:11], v[56:57], v[14:15] op_sel_hi:[1,0]
	v_exp_f32_e32 v4, v4
	v_exp_f32_e32 v5, v5
	v_exp_f32_e32 v6, v6
	v_exp_f32_e32 v7, v7
	v_exp_f32_e32 v8, v8
	v_exp_f32_e32 v9, v9
	v_exp_f32_e32 v10, v10
	v_exp_f32_e32 v11, v11
	v_pk_add_f32 v[4:5], v[4:5], v[20:21] op_sel_hi:[1,0]
	v_pk_add_f32 v[6:7], v[6:7], v[20:21] op_sel_hi:[1,0]
	v_pk_add_f32 v[8:9], v[8:9], v[20:21] op_sel_hi:[1,0]
	v_pk_add_f32 v[10:11], v[10:11], v[20:21] op_sel_hi:[1,0]
	v_rcp_f32_e32 v4, v4
	v_rcp_f32_e32 v5, v5
	v_rcp_f32_e32 v6, v6
	v_rcp_f32_e32 v7, v7
	v_rcp_f32_e32 v8, v8
	v_rcp_f32_e32 v9, v9
	v_rcp_f32_e32 v10, v10
	v_rcp_f32_e32 v11, v11
	v_pk_mul_f32 v[4:5], v[62:63], v[4:5]
	v_pk_mul_f32 v[6:7], v[64:65], v[6:7]
	v_pk_mul_f32 v[8:9], v[54:55], v[8:9]
	v_pk_mul_f32 v[10:11], v[56:57], v[10:11]
	v_pk_mul_f32 v[4:5], v[58:59], v[4:5]
	v_pk_mul_f32 v[6:7], v[60:61], v[6:7]
	v_pk_mul_f32 v[8:9], v[50:51], v[8:9]
	v_pk_mul_f32 v[10:11], v[52:53], v[10:11]
	v_pk_mul_f32 v[4:5], v[4:5], v[16:17] op_sel_hi:[1,0]
	v_pk_mul_f32 v[6:7], v[6:7], v[16:17] op_sel_hi:[1,0]
	v_pk_mul_f32 v[8:9], v[8:9], v[16:17] op_sel_hi:[1,0]
	v_pk_mul_f32 v[10:11], v[10:11], v[16:17] op_sel_hi:[1,0]
	v_med3_f32 v4, v4, s64, v250
	v_med3_f32 v5, v5, s64, v250
	v_med3_f32 v6, v6, s64, v250
	v_med3_f32 v7, v7, s64, v250
	v_med3_f32 v8, v8, s64, v250
	v_med3_f32 v9, v9, s64, v250
	v_med3_f32 v10, v10, s64, v250
	v_med3_f32 v11, v11, s64, v250
	v_cvt_pk_fp8_f32 v12, v4, v5
	v_cvt_pk_fp8_f32 v13, v8, v9
	s_nop 0
	v_cvt_pk_fp8_f32 v12, v6, v7 op_sel:[0,0,1]
	v_cvt_pk_fp8_f32 v13, v10, v11 op_sel:[0,0,1]
	v_add_u32_e32 v18, 0xa0, v0
	v_mad_i64_i32 v[18:19], s[22:23], v18, s73, v[2:3]
	global_store_dwordx2 v[18:19], v[12:13], off
	v_pk_mul_f32 v[4:5], v[46:47], v[14:15] op_sel_hi:[1,0]
	v_pk_mul_f32 v[6:7], v[48:49], v[14:15] op_sel_hi:[1,0]
	v_pk_mul_f32 v[8:9], v[38:39], v[14:15] op_sel_hi:[1,0]
	v_pk_mul_f32 v[10:11], v[40:41], v[14:15] op_sel_hi:[1,0]
	v_exp_f32_e32 v4, v4
	v_exp_f32_e32 v5, v5
	v_exp_f32_e32 v6, v6
	v_exp_f32_e32 v7, v7
	v_exp_f32_e32 v8, v8
	v_exp_f32_e32 v9, v9
	v_exp_f32_e32 v10, v10
	v_exp_f32_e32 v11, v11
	v_pk_add_f32 v[4:5], v[4:5], v[20:21] op_sel_hi:[1,0]
	v_pk_add_f32 v[6:7], v[6:7], v[20:21] op_sel_hi:[1,0]
	v_pk_add_f32 v[8:9], v[8:9], v[20:21] op_sel_hi:[1,0]
	v_pk_add_f32 v[10:11], v[10:11], v[20:21] op_sel_hi:[1,0]
	v_rcp_f32_e32 v4, v4
	v_rcp_f32_e32 v5, v5
	v_rcp_f32_e32 v6, v6
	v_rcp_f32_e32 v7, v7
	v_rcp_f32_e32 v8, v8
	v_rcp_f32_e32 v9, v9
	v_rcp_f32_e32 v10, v10
	v_rcp_f32_e32 v11, v11
	v_pk_mul_f32 v[4:5], v[46:47], v[4:5]
	v_pk_mul_f32 v[6:7], v[48:49], v[6:7]
	v_pk_mul_f32 v[8:9], v[38:39], v[8:9]
	v_pk_mul_f32 v[10:11], v[40:41], v[10:11]
	v_pk_mul_f32 v[4:5], v[42:43], v[4:5]
	v_pk_mul_f32 v[6:7], v[44:45], v[6:7]
	v_pk_mul_f32 v[8:9], v[34:35], v[8:9]
	v_pk_mul_f32 v[10:11], v[36:37], v[10:11]
	v_pk_mul_f32 v[4:5], v[4:5], v[16:17] op_sel_hi:[1,0]
	v_pk_mul_f32 v[6:7], v[6:7], v[16:17] op_sel_hi:[1,0]
	v_pk_mul_f32 v[8:9], v[8:9], v[16:17] op_sel_hi:[1,0]
	v_pk_mul_f32 v[10:11], v[10:11], v[16:17] op_sel_hi:[1,0]
	v_med3_f32 v4, v4, s64, v250
	v_med3_f32 v5, v5, s64, v250
	v_med3_f32 v6, v6, s64, v250
	v_med3_f32 v7, v7, s64, v250
	v_med3_f32 v8, v8, s64, v250
	v_med3_f32 v9, v9, s64, v250
	v_med3_f32 v10, v10, s64, v250
	v_med3_f32 v11, v11, s64, v250
	v_cvt_pk_fp8_f32 v12, v4, v5
	v_cvt_pk_fp8_f32 v13, v8, v9
	s_nop 0
	v_cvt_pk_fp8_f32 v12, v6, v7 op_sel:[0,0,1]
	v_cvt_pk_fp8_f32 v13, v10, v11 op_sel:[0,0,1]
	v_add_u32_e32 v0, 0xb0, v0
	v_mad_i64_i32 v[2:3], s[22:23], v0, s73, v[2:3]
	s_mov_b64 s[22:23], -1
	s_and_b64 vcc, exec, s[2:3]
	global_store_dwordx2 v[2:3], v[12:13], off
	s_cbranch_vccnz .LBB0_1358
	s_andn2_b64 vcc, exec, s[14:15]
	s_cbranch_vccnz .LBB0_1357
	s_barrier
	s_branch .LBB0_1357
